# v40 minus the four s_nop 0 hazard pads after the PV-head inline-asm waits in the attention hot loops
# baseline (speedup 1.0000x reference)
.Lcw_a_done:
	s_mov_b32 s1, s97
	s_mov_b32 m0, s86
	s_add_i32 s5, s0, 0xffff2000
	ds_read_b128 v[0:3], v190 offset:32768
	ds_read_b128 v[112:115], v190 offset:40960
	buffer_load_dwordx4 v191, s[68:71], s5 offen lds
	ds_read_b128 v[4:7], v189 offset:32768
	ds_read_b128 v[116:119], v189 offset:40960
	s_add_i32 s6, s0, 0xffff4000
	s_mov_b32 m0, s85
	s_waitcnt lgkmcnt(3)
	v_mfma_f32_32x32x16_f16 v[80:95], v[0:3], v[156:159], -0.5
	s_add_i32 s7, s0, 0xffff6000
	buffer_load_dwordx4 v191, s[68:71], s6 offen lds
	s_waitcnt lgkmcnt(1)
	v_mfma_f32_32x32x16_f16 v[80:95], v[4:7], v[152:155], v[80:95]
	v_mfma_f32_32x32x16_f16 v[0:15], v[112:115], v[156:159], -0.5
	ds_read_b128 v[112:115], v188 offset:32768
	s_mov_b32 m0, s84
	s_add_i32 s9, s0, 0xffff8000
	s_add_i32 s10, s0, 0xfffea000
	v_exp_f32_e32 v182, v100
	v_exp_f32_e32 v183, v101
	s_waitcnt lgkmcnt(1)
	v_mfma_f32_32x32x16_f16 v[0:15], v[116:119], v[152:155], v[0:15]
	ds_read_b128 v[116:119], v188 offset:40960
	buffer_load_dwordx4 v191, s[68:71], s7 offen lds
	s_mov_b32 m0, s83
	v_exp_f32_e32 v192, v106
	v_exp_f32_e32 v193, v107
	v_exp_f32_e32 v194, v108
	v_exp_f32_e32 v111, v111
	s_waitcnt lgkmcnt(1)
	v_mfma_f32_32x32x16_f16 v[80:95], v[112:115], v[148:151], v[80:95]
	ds_read_b128 v[112:115], v187 offset:32768
	ds_read_b128 v[120:123], v187 offset:40960
	buffer_load_dwordx4 v191, s[68:71], s9 offen lds
	s_mov_b32 m0, s90
	ds_read_b128 v[124:127], v190 offset:32896
	ds_read_b128 v[162:165], v190 offset:41088
	buffer_load_dwordx4 v186, s[72:75], s10 offen lds
	s_add_i32 s10, s0, 0xfffec000
	s_mov_b32 m0, s89
	s_waitcnt lgkmcnt(4)
	v_mfma_f32_32x32x16_f16 v[0:15], v[116:119], v[148:151], v[0:15]
	ds_read_b128 v[116:119], v189 offset:32896
	ds_read_b128 v[166:169], v189 offset:41088
	buffer_load_dwordx4 v186, s[72:75], s10 offen lds
	s_add_i32 s10, s0, 0xfffee000
	s_mov_b32 m0, s88
	v_cvt_pk_f16_f32 v100, v218, v219
	v_cvt_pk_f16_f32 v101, v220, v221
	v_cvt_pk_f16_f32 v106, v182, v183
	s_waitcnt lgkmcnt(5)
	v_mfma_f32_32x32x16_f16 v[80:95], v[112:115], v[144:147], v[80:95]
	ds_read_b128 v[112:115], v188 offset:32896
	ds_read_b128 v[170:173], v188 offset:41088
	buffer_load_dwordx4 v186, s[72:75], s10 offen lds
	s_add_i32 s10, s0, 0xffff0000
	s_mov_b32 m0, s87
	ds_read_b128 v[174:177], v187 offset:32896
	ds_read_b128 v[178:181], v187 offset:41088
	buffer_load_dwordx4 v186, s[72:75], s10 offen lds
	s_waitcnt lgkmcnt(8)
	v_mfma_f32_32x32x16_f16 v[0:15], v[120:123], v[144:147], v[0:15]
	v_exp_f32_e32 v120, v96
	v_add_f32_e32 v96, 0, v210
	v_add_f32_e32 v96, v211, v96
	v_add_f32_e32 v96, v212, v96
	v_add_f32_e32 v96, v213, v96
	v_add_f32_e32 v96, v214, v96
	v_add_f32_e32 v96, v215, v96
	s_waitcnt lgkmcnt(7)
	v_mfma_f32_32x32x16_f16 v[80:95], v[124:127], v[140:143], v[80:95]
	v_add_f32_e32 v96, v216, v96
	v_add_f32_e32 v96, v217, v96
	v_add_f32_e32 v96, v218, v96
	v_add_f32_e32 v96, v219, v96
	v_add_f32_e32 v96, v220, v96
	v_add_f32_e32 v96, v221, v96
	v_add_f32_e32 v96, v222, v96
	v_exp_f32_e32 v121, v97
	s_waitcnt lgkmcnt(6)
	v_mfma_f32_32x32x16_f16 v[0:15], v[162:165], v[140:143], v[0:15]
	v_add_f32_e32 v96, v223, v96
	v_exp_f32_e32 v122, v98
	v_add_f32_e32 v96, v224, v96
	v_exp_f32_e32 v123, v99
	v_add_f32_e32 v96, v225, v96
	v_add_f32_e32 v96, v120, v96
	v_add_f32_e32 v96, v121, v96
	s_waitcnt lgkmcnt(5)
	v_mfma_f32_32x32x16_f16 v[80:95], v[116:119], v[136:139], v[80:95]
	v_exp_f32_e32 v124, v102
	v_add_f32_e32 v96, v122, v96
	v_exp_f32_e32 v125, v103
	v_add_f32_e32 v96, v123, v96
	v_exp_f32_e32 v126, v104
	v_add_f32_e32 v96, v182, v96
	v_exp_f32_e32 v127, v105
	s_waitcnt lgkmcnt(4)
	v_mfma_f32_32x32x16_f16 v[0:15], v[166:169], v[136:139], v[0:15]
	v_add_f32_e32 v96, v183, v96
	v_add_f32_e32 v96, v124, v96
	v_add_f32_e32 v96, v125, v96
	v_add_f32_e32 v96, v126, v96
	v_exp_f32_e32 v162, v109
	v_add_f32_e32 v96, v127, v96
	v_exp_f32_e32 v163, v110
	s_waitcnt lgkmcnt(3)
	v_mfma_f32_32x32x16_f16 v[80:95], v[112:115], v[132:135], v[80:95]
	v_add_f32_e32 v96, v192, v96
	v_add_f32_e32 v96, v193, v96
	v_add_f32_e32 v96, v194, v96
	v_add_f32_e32 v96, v162, v96
	v_add_f32_e32 v96, v163, v96
	v_add_f32_e32 v96, v111, v96
	v_mov_b32_e32 v97, v96
	s_waitcnt lgkmcnt(2)
	v_mfma_f32_32x32x16_f16 v[0:15], v[170:173], v[132:135], v[0:15]
	v_permlane32_swap_b32_e32 v96, v97
	v_add_f32_e32 v96, v96, v97
	v_add_f32_e32 v185, v185, v96
	v_cvt_pk_f16_f32 v96, v210, v211
	v_cvt_pk_f16_f32 v97, v212, v213
	v_cvt_pk_f16_f32 v98, v214, v215
	s_waitcnt lgkmcnt(1)
	v_mfma_f32_32x32x16_f16 v[80:95], v[174:177], v[128:131], v[80:95]
	v_cvt_pk_f16_f32 v99, v216, v217
	v_cvt_pk_f16_f32 v102, v222, v223
	v_cvt_pk_f16_f32 v103, v224, v225
	v_cvt_pk_f16_f32 v104, v120, v121
	v_cvt_pk_f16_f32 v105, v122, v123
	v_cvt_pk_f16_f32 v107, v124, v125
	v_cvt_pk_f16_f32 v108, v126, v127
	v_cvt_pk_f16_f32 v109, v192, v193
	v_cvt_pk_f16_f32 v110, v194, v162
	v_cvt_pk_f16_f32 v111, v163, v111
	v_permlane32_swap_b32_e32 v96, v98
	v_permlane32_swap_b32_e32 v97, v99
	v_permlane32_swap_b32_e32 v100, v102
	v_permlane32_swap_b32_e32 v101, v103
	v_permlane32_swap_b32_e32 v104, v106
	v_permlane32_swap_b32_e32 v105, v107
	v_permlane32_swap_b32_e32 v108, v110
	v_permlane32_swap_b32_e32 v109, v111
	s_waitcnt lgkmcnt(0)
	v_mfma_f32_32x32x16_f16 v[0:15], v[178:181], v[128:131], v[0:15]
	ds_read_b64_tr_b16 v[112:113], v184 offset:0
	ds_read_b64_tr_b16 v[114:115], v184 offset:0x800
	ds_read_b64_tr_b16 v[116:117], v184 offset:0x1000
	ds_read_b64_tr_b16 v[118:119], v184 offset:0x1800
	ds_read_b64_tr_b16 v[120:121], v184 offset:0x2000
	ds_read_b64_tr_b16 v[122:123], v184 offset:0x2800
	ds_read_b64_tr_b16 v[124:125], v184 offset:0x3000
	ds_read_b64_tr_b16 v[126:127], v184 offset:0x3800
	s_waitcnt lgkmcnt(0)
	v_mfma_f32_32x32x16_f16 v[64:79], v[96:99], v[112:115], v[64:79]
	v_exp_f32_e32 v208, v80
	v_exp_f32_e32 v192, v81
	ds_read_b64_tr_b16 v[80:81], v184 offset:0x200
	v_exp_f32_e32 v193, v82
	v_exp_f32_e32 v194, v83
	ds_read_b64_tr_b16 v[82:83], v184 offset:0xa00
	ds_read_b64_tr_b16 v[112:113], v184 offset:0x1200
	v_mfma_f32_32x32x16_f16 v[64:79], v[100:103], v[116:119], v[64:79]
	ds_read_b64_tr_b16 v[114:115], v184 offset:0x1a00
	ds_read_b64_tr_b16 v[116:117], v184 offset:0x2200
	ds_read_b64_tr_b16 v[118:119], v184 offset:0x2a00
	v_mfma_f32_32x32x16_f16 v[64:79], v[104:107], v[120:123], v[64:79]
	ds_read_b64_tr_b16 v[120:121], v184 offset:0x3200
	ds_read_b64_tr_b16 v[122:123], v184 offset:0x3a00
	v_mfma_f32_32x32x16_f16 v[64:79], v[108:111], v[124:127], v[64:79]
	s_waitcnt lgkmcnt(0)
	v_mfma_f32_32x32x16_f16 v[48:63], v[96:99], v[80:83], v[48:63]
	ds_read_b64_tr_b16 v[80:81], v184 offset:0x400
	ds_read_b64_tr_b16 v[82:83], v184 offset:0xc00
	v_exp_f32_e32 v195, v84
	v_exp_f32_e32 v196, v85
	ds_read_b64_tr_b16 v[84:85], v184 offset:0x1400
	v_exp_f32_e32 v197, v86
	v_exp_f32_e32 v198, v87
	v_mfma_f32_32x32x16_f16 v[48:63], v[100:103], v[112:115], v[48:63]
	ds_read_b64_tr_b16 v[86:87], v184 offset:0x1c00
	ds_read_b64_tr_b16 v[112:113], v184 offset:0x2400
	ds_read_b64_tr_b16 v[114:115], v184 offset:0x2c00
	v_mfma_f32_32x32x16_f16 v[48:63], v[104:107], v[116:119], v[48:63]
	ds_read_b64_tr_b16 v[116:117], v184 offset:0x3400
	ds_read_b64_tr_b16 v[118:119], v184 offset:0x3c00
	v_mfma_f32_32x32x16_f16 v[48:63], v[108:111], v[120:123], v[48:63]
	s_waitcnt lgkmcnt(0)
	v_mfma_f32_32x32x16_f16 v[32:47], v[96:99], v[80:83], v[32:47]
	ds_read_b64_tr_b16 v[80:81], v184 offset:0x600
	ds_read_b64_tr_b16 v[82:83], v184 offset:0xe00
	v_exp_f32_e32 v199, v88
	v_exp_f32_e32 v200, v89
	v_exp_f32_e32 v201, v90
	v_exp_f32_e32 v202, v91
	v_mfma_f32_32x32x16_f16 v[32:47], v[100:103], v[84:87], v[32:47]
	ds_read_b64_tr_b16 v[84:85], v184 offset:0x1600
	ds_read_b64_tr_b16 v[86:87], v184 offset:0x1e00
	ds_read_b64_tr_b16 v[88:89], v184 offset:0x2600
	ds_read_b64_tr_b16 v[90:91], v184 offset:0x2e00
	v_mfma_f32_32x32x16_f16 v[32:47], v[104:107], v[112:115], v[32:47]
	ds_read_b64_tr_b16 v[112:113], v184 offset:0x3600
	ds_read_b64_tr_b16 v[114:115], v184 offset:0x3e00
	v_mfma_f32_32x32x16_f16 v[32:47], v[108:111], v[116:119], v[32:47]
	s_waitcnt lgkmcnt(0)
	v_mfma_f32_32x32x16_f16 v[16:31], v[96:99], v[80:83], v[16:31]
	v_exp_f32_e32 v203, v92
	v_exp_f32_e32 v204, v93
	v_exp_f32_e32 v205, v94
	v_exp_f32_e32 v206, v95
	s_waitcnt vmcnt(0) lgkmcnt(0)
	s_barrier
	v_mfma_f32_32x32x16_f16 v[16:31], v[100:103], v[84:87], v[16:31]
	v_mfma_f32_32x32x16_f16 v[16:31], v[104:107], v[88:91], v[16:31]
	v_mfma_f32_32x32x16_f16 v[16:31], v[108:111], v[112:115], v[16:31]
	s_cmp_gt_u32 s100, 8
	s_cbranch_scc1 .Lcw_b_done
	s_cmp_eq_u32 s100, 0
	s_cbranch_scc1 .Lcw_b_load
	v_cvt_pk_f16_f32 v252, v252, v253
	v_cvt_pk_f16_f32 v253, v254, v255
	v_lshrrev_b32_e32 v254, 1, v191
	global_store_dwordx2 v254, v[252:253], s[60:61]
	s_add_u32 s60, s60, 0x1000
	s_addc_u32 s61, s61, 0
	s_cmp_eq_u32 s100, 8
	s_cbranch_scc1 .Lcw_b_inc

.Lcw_b_done:
	s_mov_b32 m0, s91
	s_add_i32 s10, s0, 0xffffa000
	ds_read_b128 v[80:83], v190
	ds_read_b128 v[84:87], v190 offset:8192
	buffer_load_dwordx4 v191, s[68:71], s10 offen lds
	ds_read_b128 v[88:91], v189
	ds_read_b128 v[92:95], v189 offset:8192
	s_add_i32 s10, s0, 0xffffc000
	s_mov_b32 m0, s92
	s_waitcnt lgkmcnt(3)
	v_mfma_f32_32x32x16_f16 v[112:127], v[80:83], v[156:159], -0.5
	s_waitcnt lgkmcnt(2)
	v_mfma_f32_32x32x16_f16 v[96:111], v[84:87], v[156:159], -0.5
	buffer_load_dwordx4 v191, s[68:71], s10 offen lds
	ds_read_b128 v[80:83], v188
	ds_read_b128 v[84:87], v188 offset:8192
	s_waitcnt lgkmcnt(3)
	v_mfma_f32_32x32x16_f16 v[112:127], v[88:91], v[152:155], v[112:127]
	s_add_i32 s10, s0, 0xffffe000
	s_mov_b32 m0, s93
	s_nop 0
	buffer_load_dwordx4 v191, s[68:71], s10 offen lds
	s_mov_b32 m0, s94
	s_waitcnt lgkmcnt(1)
	v_mfma_f32_32x32x16_f16 v[112:127], v[80:83], v[148:151], v[112:127]
	ds_read_b128 v[80:83], v187
	ds_read_b128 v[88:91], v187 offset:8192
	buffer_load_dwordx4 v191, s[68:71], s0 offen lds
	s_mov_b32 m0, s3
	v_mfma_f32_32x32x16_f16 v[96:111], v[92:95], v[152:155], v[96:111]
	ds_read_b128 v[92:95], v190 offset:128
	ds_read_b128 v[162:165], v190 offset:8320
	buffer_load_dwordx4 v186, s[72:75], s5 offen lds
	s_mov_b32 m0, s82
	ds_read_b128 v[166:169], v189 offset:128
	ds_read_b128 v[170:173], v189 offset:8320
	buffer_load_dwordx4 v186, s[72:75], s6 offen lds
	s_mov_b32 m0, s81
	ds_read_b128 v[174:177], v188 offset:128
	ds_read_b128 v[178:181], v188 offset:8320
	buffer_load_dwordx4 v186, s[72:75], s7 offen lds
	s_mov_b32 m0, s80
	ds_read_b128 v[210:213], v187 offset:128
	ds_read_b128 v[214:217], v187 offset:8320
	buffer_load_dwordx4 v186, s[72:75], s9 offen lds
	s_waitcnt lgkmcnt(10)
	v_mfma_f32_32x32x16_f16 v[96:111], v[84:87], v[148:151], v[96:111]
	v_exp_f32_e32 v84, v4
	v_exp_f32_e32 v85, v5
	v_exp_f32_e32 v86, v6
	v_exp_f32_e32 v87, v7
	v_cvt_pk_f16_f32 v4, v199, v200
	v_cvt_pk_f16_f32 v5, v201, v202
	v_cvt_pk_f16_f32 v6, v203, v204
	s_waitcnt lgkmcnt(8)
	v_mfma_f32_32x32x16_f16 v[96:111], v[88:91], v[144:147], v[96:111]
	v_exp_f32_e32 v88, v8
	v_exp_f32_e32 v89, v9
	v_exp_f32_e32 v90, v10
	v_exp_f32_e32 v91, v11
	v_cvt_pk_f16_f32 v7, v205, v206
	v_cvt_pk_f16_f32 v10, v84, v85
	v_cvt_pk_f16_f32 v11, v86, v87
	v_mfma_f32_32x32x16_f16 v[112:127], v[80:83], v[144:147], v[112:127]
	v_exp_f32_e32 v80, v0
	v_add_f32_e32 v0, 0, v208
	v_add_f32_e32 v0, v192, v0
	v_add_f32_e32 v0, v193, v0
	v_add_f32_e32 v0, v194, v0
	v_add_f32_e32 v0, v195, v0
	v_add_f32_e32 v0, v196, v0
	s_waitcnt lgkmcnt(6)
	v_mfma_f32_32x32x16_f16 v[96:111], v[162:165], v[140:143], v[96:111]
	v_add_f32_e32 v0, v197, v0
	v_add_f32_e32 v0, v198, v0
	v_add_f32_e32 v0, v199, v0
	v_add_f32_e32 v0, v200, v0
	v_add_f32_e32 v0, v201, v0
	v_add_f32_e32 v0, v202, v0
	v_add_f32_e32 v0, v203, v0
	v_mfma_f32_32x32x16_f16 v[112:127], v[92:95], v[140:143], v[112:127]
	v_exp_f32_e32 v81, v1
	v_add_f32_e32 v0, v204, v0
	v_exp_f32_e32 v82, v2
	v_add_f32_e32 v0, v205, v0
	v_exp_f32_e32 v83, v3
	v_add_f32_e32 v0, v206, v0
	v_add_f32_e32 v0, v80, v0
	s_waitcnt lgkmcnt(4)
	v_mfma_f32_32x32x16_f16 v[96:111], v[170:173], v[136:139], v[96:111]
	v_add_f32_e32 v0, v81, v0
	v_add_f32_e32 v0, v82, v0
	v_add_f32_e32 v0, v83, v0
	v_add_f32_e32 v0, v84, v0
	v_add_f32_e32 v0, v85, v0
	v_add_f32_e32 v0, v86, v0
	v_add_f32_e32 v0, v87, v0
	v_mfma_f32_32x32x16_f16 v[112:127], v[166:169], v[136:139], v[112:127]
	v_exp_f32_e32 v92, v12
	v_add_f32_e32 v0, v88, v0
	v_exp_f32_e32 v93, v13
	v_add_f32_e32 v0, v89, v0
	v_exp_f32_e32 v94, v14
	v_add_f32_e32 v0, v90, v0
	v_exp_f32_e32 v95, v15
	s_waitcnt lgkmcnt(2)
	v_mfma_f32_32x32x16_f16 v[96:111], v[178:181], v[132:135], v[96:111]
	v_add_f32_e32 v0, v91, v0
	v_add_f32_e32 v0, v92, v0
	v_add_f32_e32 v0, v93, v0
	v_add_f32_e32 v0, v94, v0
	v_add_f32_e32 v0, v95, v0
	v_mov_b32_e32 v1, v0
	s_nop 1
	v_permlane32_swap_b32_e32 v0, v1
	v_mfma_f32_32x32x16_f16 v[112:127], v[174:177], v[132:135], v[112:127]
	v_add_f32_e32 v0, v0, v1
	v_add_f32_e32 v185, v185, v0
	v_cvt_pk_f16_f32 v0, v208, v192
	v_cvt_pk_f16_f32 v1, v193, v194
	v_cvt_pk_f16_f32 v2, v195, v196
	v_cvt_pk_f16_f32 v3, v197, v198
	v_cvt_pk_f16_f32 v8, v80, v81
	s_waitcnt lgkmcnt(0)
	v_mfma_f32_32x32x16_f16 v[96:111], v[214:217], v[128:131], v[96:111]
	v_cvt_pk_f16_f32 v9, v82, v83
	v_cvt_pk_f16_f32 v12, v88, v89
	v_cvt_pk_f16_f32 v13, v90, v91
	v_cvt_pk_f16_f32 v14, v92, v93
	v_cvt_pk_f16_f32 v15, v94, v95
	v_permlane32_swap_b32_e32 v0, v2
	v_mfma_f32_32x32x16_f16 v[112:127], v[210:213], v[128:131], v[112:127]
	v_permlane32_swap_b32_e32 v1, v3
	v_permlane32_swap_b32_e32 v4, v6
	v_permlane32_swap_b32_e32 v5, v7
	v_permlane32_swap_b32_e32 v8, v10
	v_permlane32_swap_b32_e32 v9, v11
	v_permlane32_swap_b32_e32 v12, v14
	v_permlane32_swap_b32_e32 v13, v15
	ds_read_b64_tr_b16 v[162:163], v184 offset:0x8000
	ds_read_b64_tr_b16 v[164:165], v184 offset:0x8800
	ds_read_b64_tr_b16 v[166:167], v184 offset:0x9000
	ds_read_b64_tr_b16 v[168:169], v184 offset:0x9800
	ds_read_b64_tr_b16 v[170:171], v184 offset:0xa000
	ds_read_b64_tr_b16 v[172:173], v184 offset:0xa800
	ds_read_b64_tr_b16 v[174:175], v184 offset:0xb000
	ds_read_b64_tr_b16 v[176:177], v184 offset:0xb800
	s_waitcnt lgkmcnt(0)
	v_mfma_f32_32x32x16_f16 v[64:79], v[0:3], v[162:165], v[64:79]
	s_nop 2
	v_exp_f32_e32 v210, v112
	v_exp_f32_e32 v211, v113
	ds_read_b64_tr_b16 v[112:113], v184 offset:0x8200
	v_exp_f32_e32 v212, v114
	v_exp_f32_e32 v213, v115
	ds_read_b64_tr_b16 v[114:115], v184 offset:0x8a00
	ds_read_b64_tr_b16 v[162:163], v184 offset:0x9200
	v_mfma_f32_32x32x16_f16 v[64:79], v[4:7], v[166:169], v[64:79]
	ds_read_b64_tr_b16 v[164:165], v184 offset:0x9a00
	ds_read_b64_tr_b16 v[166:167], v184 offset:0xa200
	ds_read_b64_tr_b16 v[168:169], v184 offset:0xaa00
	v_mfma_f32_32x32x16_f16 v[64:79], v[8:11], v[170:173], v[64:79]
	ds_read_b64_tr_b16 v[170:171], v184 offset:0xb200
	ds_read_b64_tr_b16 v[172:173], v184 offset:0xba00
	v_mfma_f32_32x32x16_f16 v[64:79], v[12:15], v[174:177], v[64:79]
	s_waitcnt lgkmcnt(0)
	v_mfma_f32_32x32x16_f16 v[48:63], v[0:3], v[112:115], v[48:63]
	ds_read_b64_tr_b16 v[112:113], v184 offset:0x8400
	ds_read_b64_tr_b16 v[114:115], v184 offset:0x8c00
	v_exp_f32_e32 v214, v116
	v_exp_f32_e32 v215, v117
	ds_read_b64_tr_b16 v[116:117], v184 offset:0x9400
	v_exp_f32_e32 v216, v118
	v_exp_f32_e32 v217, v119
	v_mfma_f32_32x32x16_f16 v[48:63], v[4:7], v[162:165], v[48:63]
	ds_read_b64_tr_b16 v[118:119], v184 offset:0x9c00
	ds_read_b64_tr_b16 v[162:163], v184 offset:0xa400
	ds_read_b64_tr_b16 v[164:165], v184 offset:0xac00
	v_mfma_f32_32x32x16_f16 v[48:63], v[8:11], v[166:169], v[48:63]
	ds_read_b64_tr_b16 v[166:167], v184 offset:0xb400
	ds_read_b64_tr_b16 v[168:169], v184 offset:0xbc00
	v_mfma_f32_32x32x16_f16 v[48:63], v[12:15], v[170:173], v[48:63]
	s_waitcnt lgkmcnt(0)
	v_mfma_f32_32x32x16_f16 v[32:47], v[0:3], v[112:115], v[32:47]
	ds_read_b64_tr_b16 v[112:113], v184 offset:0x8600
	ds_read_b64_tr_b16 v[114:115], v184 offset:0x8e00
	v_exp_f32_e32 v218, v120
	v_exp_f32_e32 v219, v121
	v_exp_f32_e32 v220, v122
	v_exp_f32_e32 v221, v123
	v_mfma_f32_32x32x16_f16 v[32:47], v[4:7], v[116:119], v[32:47]
	ds_read_b64_tr_b16 v[116:117], v184 offset:0x9600
	ds_read_b64_tr_b16 v[118:119], v184 offset:0x9e00
	ds_read_b64_tr_b16 v[120:121], v184 offset:0xa600
	ds_read_b64_tr_b16 v[122:123], v184 offset:0xae00
	v_mfma_f32_32x32x16_f16 v[32:47], v[8:11], v[162:165], v[32:47]
	ds_read_b64_tr_b16 v[162:163], v184 offset:0xb600
	ds_read_b64_tr_b16 v[164:165], v184 offset:0xbe00
	v_mfma_f32_32x32x16_f16 v[32:47], v[12:15], v[166:169], v[32:47]
	s_waitcnt lgkmcnt(0)
	v_mfma_f32_32x32x16_f16 v[16:31], v[0:3], v[112:115], v[16:31]
	v_exp_f32_e32 v222, v124
	v_exp_f32_e32 v223, v125
	v_exp_f32_e32 v224, v126
	v_exp_f32_e32 v225, v127
	s_waitcnt vmcnt(0) lgkmcnt(0)
	s_barrier
	v_mfma_f32_32x32x16_f16 v[16:31], v[4:7], v[116:119], v[16:31]
	v_mfma_f32_32x32x16_f16 v[16:31], v[8:11], v[120:123], v[16:31]
	v_mfma_f32_32x32x16_f16 v[16:31], v[12:15], v[162:165], v[16:31]
	s_add_i32 s97, s97, 2
	s_add_i32 s1, s1, 4
	s_add_i32 s0, s0, 0x10000
	s_cmp_le_u32 s1, s99
	s_cbranch_scc1 .LBB3_3
	v_mul_i32_i24_e32 v0, -4, v160
	s_lshl_b32 s0, s4, 6
	v_subrev_u32_e32 v209, s0, v0
	s_cmp_gt_u32 s97, s99
	v_add_u32_e32 v160, v209, v161
	s_cbranch_scc1 .LBB3_18
	s_cmp_lt_u32 s97, s99
	s_cselect_b64 s[6:7], -1, 0
	s_cmp_ge_u32 s97, s99
	s_cselect_b64 s[4:5], -1, 0
	ds_read_b128 v[80:83], v190 offset:32768
	ds_read_b128 v[112:115], v190 offset:40960
	s_and_b64 vcc, exec, s[4:5]
	s_waitcnt lgkmcnt(1)
	v_mfma_f32_32x32x16_f16 v[0:15], v[80:83], v[156:159], -0.5
	s_waitcnt lgkmcnt(0)
	v_mfma_f32_32x32x16_f16 v[80:95], v[112:115], v[156:159], -0.5
	s_cbranch_vccnz .LBB3_7
	s_lshl_b32 s0, s97, 15
	s_add_i32 s0, s0, 0x8000
	s_mov_b32 m0, s86
	s_nop 0
	buffer_load_dwordx4 v191, s[68:71], s0 offen lds

.LBB3_44:
	s_mov_b32 s5, s99
	s_mov_b32 m0, s86
	s_add_i32 s6, s4, 0xffff2000
	ds_read_b128 v[0:3], v190 offset:32768
	ds_read_b128 v[82:85], v190 offset:40960
	buffer_load_dwordx4 v191, s[68:71], s6 offen lds
	ds_read_b128 v[4:7], v189 offset:32768
	ds_read_b128 v[86:89], v189 offset:40960
	s_add_i32 s7, s4, 0xffff4000
	s_mov_b32 m0, s85
	s_waitcnt lgkmcnt(3)
	v_mfma_f32_32x32x16_f16 v[112:127], v[0:3], v[156:159], -0.5
	s_add_i32 s8, s4, 0xffff6000
	buffer_load_dwordx4 v191, s[68:71], s7 offen lds
	s_waitcnt lgkmcnt(1)
	v_mfma_f32_32x32x16_f16 v[112:127], v[4:7], v[152:155], v[112:127]
	v_mfma_f32_32x32x16_f16 v[0:15], v[82:85], v[156:159], -0.5
	ds_read_b128 v[82:85], v188 offset:32768
	s_mov_b32 m0, s84
	s_add_i32 s9, s4, 0xffff8000
	s_add_i32 s10, s4, 0xfffea000
	v_add_f32_e32 v81, 0, v169
	v_add_f32_e32 v81, v170, v81
	s_waitcnt lgkmcnt(1)
	v_mfma_f32_32x32x16_f16 v[0:15], v[86:89], v[152:155], v[0:15]
	ds_read_b128 v[86:89], v188 offset:40960
	buffer_load_dwordx4 v191, s[68:71], s8 offen lds
	s_mov_b32 m0, s83
	v_add_f32_e32 v81, v171, v81
	v_add_f32_e32 v81, v172, v81
	v_add_f32_e32 v81, v173, v81
	v_add_f32_e32 v81, v174, v81
	s_waitcnt lgkmcnt(1)
	v_mfma_f32_32x32x16_f16 v[112:127], v[82:85], v[148:151], v[112:127]
	ds_read_b128 v[82:85], v187 offset:32768
	ds_read_b128 v[90:93], v187 offset:40960
	buffer_load_dwordx4 v191, s[68:71], s9 offen lds
	s_mov_b32 m0, s90
	ds_read_b128 v[160:163], v190 offset:32896
	ds_read_b128 v[164:167], v190 offset:41088
	buffer_load_dwordx4 v186, s[72:75], s10 offen lds
	s_add_i32 s10, s4, 0xfffec000
	s_mov_b32 m0, s89
	s_waitcnt lgkmcnt(4)
	v_mfma_f32_32x32x16_f16 v[0:15], v[86:89], v[148:151], v[0:15]
	ds_read_b128 v[86:89], v189 offset:32896
	ds_read_b128 v[192:195], v189 offset:41088
	buffer_load_dwordx4 v186, s[72:75], s10 offen lds
	s_add_i32 s10, s4, 0xfffee000
	s_mov_b32 m0, s88
	v_add_f32_e32 v81, v175, v81
	v_add_f32_e32 v81, v176, v81
	v_add_f32_e32 v81, v177, v81
	s_waitcnt lgkmcnt(5)
	v_mfma_f32_32x32x16_f16 v[112:127], v[82:85], v[144:147], v[112:127]
	ds_read_b128 v[82:85], v188 offset:32896
	ds_read_b128 v[196:199], v188 offset:41088
	buffer_load_dwordx4 v186, s[72:75], s10 offen lds
	s_add_i32 s10, s4, 0xffff0000
	s_mov_b32 m0, s87
	ds_read_b128 v[200:203], v187 offset:32896
	ds_read_b128 v[204:207], v187 offset:41088
	buffer_load_dwordx4 v186, s[72:75], s10 offen lds
	v_add_f32_e32 v81, v178, v81
	s_waitcnt lgkmcnt(8)
	v_mfma_f32_32x32x16_f16 v[0:15], v[90:93], v[144:147], v[0:15]
	v_add_f32_e32 v81, v179, v81
	v_add_f32_e32 v81, v180, v81
	v_exp_f32_e32 v90, v96
	v_add_f32_e32 v81, v181, v81
	v_exp_f32_e32 v91, v97
	v_add_f32_e32 v81, v182, v81
	v_exp_f32_e32 v92, v98
	s_waitcnt lgkmcnt(6)
	v_mfma_f32_32x32x16_f16 v[0:15], v[164:167], v[140:143], v[0:15]
	v_add_f32_e32 v81, v183, v81
	v_exp_f32_e32 v93, v99
	v_add_f32_e32 v81, v185, v81
	v_exp_f32_e32 v94, v100
	v_add_f32_e32 v81, v90, v81
	v_exp_f32_e32 v95, v101
	v_add_f32_e32 v81, v91, v81
	v_mfma_f32_32x32x16_f16 v[112:127], v[160:163], v[140:143], v[112:127]
	v_exp_f32_e32 v96, v102
	v_add_f32_e32 v81, v92, v81
	v_exp_f32_e32 v97, v103
	v_add_f32_e32 v81, v93, v81
	v_exp_f32_e32 v98, v104
	v_add_f32_e32 v81, v94, v81
	v_exp_f32_e32 v99, v105
	s_waitcnt lgkmcnt(4)
	v_mfma_f32_32x32x16_f16 v[0:15], v[192:195], v[136:139], v[0:15]
	v_add_f32_e32 v81, v95, v81
	v_exp_f32_e32 v100, v106
	v_add_f32_e32 v81, v96, v81
	v_exp_f32_e32 v101, v107
	v_add_f32_e32 v81, v97, v81
	v_exp_f32_e32 v102, v108
	v_add_f32_e32 v81, v98, v81
	v_mfma_f32_32x32x16_f16 v[112:127], v[86:89], v[136:139], v[112:127]
	v_exp_f32_e32 v103, v109
	v_add_f32_e32 v81, v99, v81
	v_exp_f32_e32 v104, v110
	v_add_f32_e32 v81, v100, v81
	v_exp_f32_e32 v105, v111
	v_add_f32_e32 v81, v101, v81
	v_add_f32_e32 v81, v102, v81
	s_waitcnt lgkmcnt(2)
	v_mfma_f32_32x32x16_f16 v[0:15], v[196:199], v[132:135], v[0:15]
	v_add_f32_e32 v81, v103, v81
	v_add_f32_e32 v81, v104, v81
	v_add_f32_e32 v81, v105, v81
	v_cvt_pk_f16_f32 v86, v181, v182
	v_cvt_pk_f16_f32 v87, v183, v185
	v_cvt_pk_f16_f32 v88, v90, v91
	v_cvt_pk_f16_f32 v89, v92, v93
	v_mfma_f32_32x32x16_f16 v[112:127], v[82:85], v[132:135], v[112:127]
	v_mov_b32_e32 v82, v81
	s_nop 1
	v_permlane32_swap_b32_e32 v81, v82
	v_add_f32_e32 v81, v81, v82
	v_add_f32_e32 v209, v80, v81
	v_cvt_pk_f16_f32 v80, v169, v170
	v_cvt_pk_f16_f32 v82, v173, v174
	s_waitcnt lgkmcnt(0)
	v_mfma_f32_32x32x16_f16 v[0:15], v[204:207], v[128:131], v[0:15]
	v_cvt_pk_f16_f32 v81, v171, v172
	v_cvt_pk_f16_f32 v83, v175, v176
	v_permlane32_swap_b32_e32 v80, v82
	v_cvt_pk_f16_f32 v84, v177, v178
	v_cvt_pk_f16_f32 v85, v179, v180
	v_cvt_pk_f16_f32 v90, v94, v95
	v_cvt_pk_f16_f32 v91, v96, v97
	v_cvt_pk_f16_f32 v92, v98, v99
	v_cvt_pk_f16_f32 v93, v100, v101
	v_cvt_pk_f16_f32 v94, v102, v103
	v_cvt_pk_f16_f32 v95, v104, v105
	v_mfma_f32_32x32x16_f16 v[112:127], v[200:203], v[128:131], v[112:127]
	v_permlane32_swap_b32_e32 v81, v83
	v_permlane32_swap_b32_e32 v84, v86
	v_permlane32_swap_b32_e32 v85, v87
	v_permlane32_swap_b32_e32 v88, v90
	v_permlane32_swap_b32_e32 v89, v91
	v_permlane32_swap_b32_e32 v92, v94
	v_permlane32_swap_b32_e32 v93, v95
	ds_read_b64_tr_b16 v[96:97], v184 offset:0
	ds_read_b64_tr_b16 v[98:99], v184 offset:0x800
	ds_read_b64_tr_b16 v[100:101], v184 offset:0x1000
	ds_read_b64_tr_b16 v[102:103], v184 offset:0x1800
	ds_read_b64_tr_b16 v[104:105], v184 offset:0x2000
	ds_read_b64_tr_b16 v[106:107], v184 offset:0x2800
	ds_read_b64_tr_b16 v[108:109], v184 offset:0x3000
	ds_read_b64_tr_b16 v[110:111], v184 offset:0x3800
	s_waitcnt lgkmcnt(0)
	v_mfma_f32_32x32x16_f16 v[64:79], v[80:83], v[96:99], v[64:79]
	ds_read_b64_tr_b16 v[96:97], v184 offset:0x200
	ds_read_b64_tr_b16 v[98:99], v184 offset:0xa00
	s_nop 2
	v_exp_f32_e32 v208, v112
	v_exp_f32_e32 v192, v113
	v_exp_f32_e32 v193, v114
	v_exp_f32_e32 v194, v115
	v_mfma_f32_32x32x16_f16 v[64:79], v[84:87], v[100:103], v[64:79]
	ds_read_b64_tr_b16 v[100:101], v184 offset:0x1200
	ds_read_b64_tr_b16 v[102:103], v184 offset:0x1a00
	v_mfma_f32_32x32x16_f16 v[64:79], v[88:91], v[104:107], v[64:79]
	ds_read_b64_tr_b16 v[104:105], v184 offset:0x2200
	ds_read_b64_tr_b16 v[106:107], v184 offset:0x2a00
	ds_read_b64_tr_b16 v[112:113], v184 offset:0x3200
	ds_read_b64_tr_b16 v[114:115], v184 offset:0x3a00
	v_mfma_f32_32x32x16_f16 v[64:79], v[92:95], v[108:111], v[64:79]
	s_waitcnt lgkmcnt(0)
	v_mfma_f32_32x32x16_f16 v[48:63], v[80:83], v[96:99], v[48:63]
	ds_read_b64_tr_b16 v[96:97], v184 offset:0x400
	ds_read_b64_tr_b16 v[98:99], v184 offset:0xc00
	v_exp_f32_e32 v195, v116
	v_exp_f32_e32 v196, v117
	v_exp_f32_e32 v197, v118
	v_exp_f32_e32 v198, v119
	v_mfma_f32_32x32x16_f16 v[48:63], v[84:87], v[100:103], v[48:63]
	ds_read_b64_tr_b16 v[100:101], v184 offset:0x1400
	ds_read_b64_tr_b16 v[102:103], v184 offset:0x1c00
	v_mfma_f32_32x32x16_f16 v[48:63], v[88:91], v[104:107], v[48:63]
	ds_read_b64_tr_b16 v[104:105], v184 offset:0x2400
	ds_read_b64_tr_b16 v[106:107], v184 offset:0x2c00
	ds_read_b64_tr_b16 v[108:109], v184 offset:0x3400
	ds_read_b64_tr_b16 v[110:111], v184 offset:0x3c00
	v_mfma_f32_32x32x16_f16 v[48:63], v[92:95], v[112:115], v[48:63]
	s_waitcnt lgkmcnt(0)
	v_mfma_f32_32x32x16_f16 v[32:47], v[80:83], v[96:99], v[32:47]
	ds_read_b64_tr_b16 v[96:97], v184 offset:0x600
	ds_read_b64_tr_b16 v[98:99], v184 offset:0xe00
	v_exp_f32_e32 v199, v120
	v_exp_f32_e32 v200, v121
	v_exp_f32_e32 v201, v122
	v_exp_f32_e32 v202, v123
	v_mfma_f32_32x32x16_f16 v[32:47], v[84:87], v[100:103], v[32:47]
	ds_read_b64_tr_b16 v[100:101], v184 offset:0x1600
	ds_read_b64_tr_b16 v[102:103], v184 offset:0x1e00
	v_mfma_f32_32x32x16_f16 v[32:47], v[88:91], v[104:107], v[32:47]
	ds_read_b64_tr_b16 v[104:105], v184 offset:0x2600
	ds_read_b64_tr_b16 v[106:107], v184 offset:0x2e00
	ds_read_b64_tr_b16 v[112:113], v184 offset:0x3600
	ds_read_b64_tr_b16 v[114:115], v184 offset:0x3e00
	v_mfma_f32_32x32x16_f16 v[32:47], v[92:95], v[108:111], v[32:47]
	s_waitcnt lgkmcnt(0)
	v_mfma_f32_32x32x16_f16 v[16:31], v[80:83], v[96:99], v[16:31]
	v_exp_f32_e32 v203, v124
	v_exp_f32_e32 v204, v125
	v_exp_f32_e32 v205, v126
	v_exp_f32_e32 v206, v127
	s_waitcnt vmcnt(0) lgkmcnt(0)
	s_barrier
	v_mfma_f32_32x32x16_f16 v[16:31], v[84:87], v[100:103], v[16:31]
	v_mfma_f32_32x32x16_f16 v[16:31], v[88:91], v[104:107], v[16:31]
	v_mfma_f32_32x32x16_f16 v[16:31], v[92:95], v[112:115], v[16:31]
	s_mov_b32 m0, s91
	s_add_i32 s10, s4, 0xffffa000
	ds_read_b128 v[80:83], v190
	ds_read_b128 v[84:87], v190 offset:8192
	buffer_load_dwordx4 v191, s[68:71], s10 offen lds
	ds_read_b128 v[88:91], v189
	ds_read_b128 v[92:95], v189 offset:8192
	s_add_i32 s10, s4, 0xffffc000
	s_mov_b32 m0, s92
	s_waitcnt lgkmcnt(3)
	v_mfma_f32_32x32x16_f16 v[112:127], v[80:83], v[156:159], -0.5
	s_waitcnt lgkmcnt(2)
	v_mfma_f32_32x32x16_f16 v[96:111], v[84:87], v[156:159], -0.5
	v_exp_f32_e32 v0, v0
	buffer_load_dwordx4 v191, s[68:71], s10 offen lds
	ds_read_b128 v[80:83], v188
	ds_read_b128 v[84:87], v188 offset:8192
	s_waitcnt lgkmcnt(3)
	v_mfma_f32_32x32x16_f16 v[112:127], v[88:91], v[152:155], v[112:127]
	s_add_i32 s10, s4, 0xffffe000
	s_mov_b32 m0, s93
	v_exp_f32_e32 v1, v1
	buffer_load_dwordx4 v191, s[68:71], s10 offen lds
	s_mov_b32 m0, s94
	v_exp_f32_e32 v2, v2
	v_exp_f32_e32 v3, v3
	s_waitcnt lgkmcnt(2)
	v_mfma_f32_32x32x16_f16 v[96:111], v[92:95], v[152:155], v[96:111]
	v_exp_f32_e32 v4, v4
	v_exp_f32_e32 v5, v5
	v_exp_f32_e32 v6, v6
	v_exp_f32_e32 v7, v7
	v_exp_f32_e32 v8, v8
	v_exp_f32_e32 v9, v9
	v_exp_f32_e32 v10, v10
	s_waitcnt lgkmcnt(1)
	v_mfma_f32_32x32x16_f16 v[112:127], v[80:83], v[148:151], v[112:127]
	ds_read_b128 v[80:83], v187
	ds_read_b128 v[88:91], v187 offset:8192
	buffer_load_dwordx4 v191, s[68:71], s4 offen lds
	s_mov_b32 m0, s3
	ds_read_b128 v[92:95], v190 offset:128
	ds_read_b128 v[160:163], v190 offset:8320
	buffer_load_dwordx4 v186, s[72:75], s6 offen lds
	s_mov_b32 m0, s82
	v_exp_f32_e32 v11, v11
	s_waitcnt lgkmcnt(4)
	v_mfma_f32_32x32x16_f16 v[96:111], v[84:87], v[148:151], v[96:111]
	ds_read_b128 v[84:87], v189 offset:128
	ds_read_b128 v[164:167], v189 offset:8320
	buffer_load_dwordx4 v186, s[72:75], s7 offen lds
	s_mov_b32 m0, s81
	ds_read_b128 v[170:173], v188 offset:128
	ds_read_b128 v[174:177], v188 offset:8320
	buffer_load_dwordx4 v186, s[72:75], s8 offen lds
	s_mov_b32 m0, s80
	v_exp_f32_e32 v12, v12
	s_waitcnt lgkmcnt(7)
	v_mfma_f32_32x32x16_f16 v[112:127], v[80:83], v[144:147], v[112:127]
	ds_read_b128 v[80:83], v187 offset:128
	ds_read_b128 v[178:181], v187 offset:8320
	buffer_load_dwordx4 v186, s[72:75], s9 offen lds
	v_exp_f32_e32 v13, v13
	v_exp_f32_e32 v14, v14
	v_exp_f32_e32 v15, v15
	s_waitcnt lgkmcnt(8)
	v_mfma_f32_32x32x16_f16 v[96:111], v[88:91], v[144:147], v[96:111]
	v_add_f32_e32 v88, 0, v208
	v_add_f32_e32 v88, v192, v88
	v_add_f32_e32 v88, v193, v88
	v_add_f32_e32 v88, v194, v88
	v_add_f32_e32 v88, v195, v88
	v_add_f32_e32 v88, v196, v88
	v_add_f32_e32 v88, v197, v88
	s_waitcnt lgkmcnt(7)
	v_mfma_f32_32x32x16_f16 v[112:127], v[92:95], v[140:143], v[112:127]
	v_add_f32_e32 v88, v198, v88
	v_cvt_pk_f16_f32 v89, v205, v206
	v_cvt_pk_f16_f32 v90, v0, v1
	v_cvt_pk_f16_f32 v91, v2, v3
	v_cvt_pk_f16_f32 v92, v4, v5
	v_cvt_pk_f16_f32 v93, v6, v7
	s_nop 0
	v_permlane32_swap_b32_e32 v90, v92
	s_waitcnt lgkmcnt(6)
	v_mfma_f32_32x32x16_f16 v[96:111], v[160:163], v[140:143], v[96:111]
	v_cvt_pk_f16_f32 v160, v8, v9
	v_cvt_pk_f16_f32 v161, v10, v11
	v_cvt_pk_f16_f32 v162, v12, v13
	v_cvt_pk_f16_f32 v163, v14, v15
	v_permlane32_swap_b32_e32 v91, v93
	v_permlane32_swap_b32_e32 v160, v162
	s_waitcnt lgkmcnt(5)
	v_mfma_f32_32x32x16_f16 v[112:127], v[84:87], v[136:139], v[112:127]
	v_add_f32_e32 v84, v199, v88
	v_add_f32_e32 v84, v200, v84
	v_add_f32_e32 v84, v201, v84
	v_add_f32_e32 v84, v202, v84
	v_add_f32_e32 v84, v203, v84
	v_add_f32_e32 v84, v204, v84
	v_add_f32_e32 v84, v205, v84
	s_waitcnt lgkmcnt(4)
	v_mfma_f32_32x32x16_f16 v[96:111], v[164:167], v[136:139], v[96:111]
	v_add_f32_e32 v84, v206, v84
	v_add_f32_e32 v84, v0, v84
	v_add_f32_e32 v84, v1, v84
	v_add_f32_e32 v84, v2, v84
	v_add_f32_e32 v84, v3, v84
	v_add_f32_e32 v84, v4, v84
	v_add_f32_e32 v84, v5, v84
	s_waitcnt lgkmcnt(2)
	v_mfma_f32_32x32x16_f16 v[96:111], v[174:177], v[132:135], v[96:111]
	v_add_f32_e32 v84, v6, v84
	v_add_f32_e32 v84, v7, v84
	v_add_f32_e32 v84, v8, v84
	v_add_f32_e32 v84, v9, v84
	v_add_f32_e32 v84, v10, v84
	v_add_f32_e32 v84, v11, v84
	v_add_f32_e32 v84, v12, v84
	v_mfma_f32_32x32x16_f16 v[112:127], v[170:173], v[132:135], v[112:127]
	v_add_f32_e32 v84, v13, v84
	v_add_f32_e32 v84, v14, v84
	v_add_f32_e32 v84, v15, v84
	v_mov_b32_e32 v85, v84
	s_nop 1
	v_permlane32_swap_b32_e32 v84, v85
	v_add_f32_e32 v84, v84, v85
	s_waitcnt lgkmcnt(0)
	v_mfma_f32_32x32x16_f16 v[96:111], v[178:181], v[128:131], v[96:111]
	v_cvt_pk_f16_f32 v85, v197, v198
	v_cvt_pk_f16_f32 v86, v199, v200
	v_cvt_pk_f16_f32 v87, v201, v202
	v_cvt_pk_f16_f32 v88, v203, v204
	s_nop 1
	v_permlane32_swap_b32_e32 v86, v88
	v_permlane32_swap_b32_e32 v87, v89
	v_mfma_f32_32x32x16_f16 v[112:127], v[80:83], v[128:131], v[112:127]
	v_add_f32_e32 v80, v209, v84
	v_cvt_pk_f16_f32 v82, v208, v192
	v_cvt_pk_f16_f32 v83, v193, v194
	v_cvt_pk_f16_f32 v84, v195, v196
	s_nop 1
	v_permlane32_swap_b32_e32 v82, v84
	v_permlane32_swap_b32_e32 v83, v85
	v_permlane32_swap_b32_e32 v161, v163
	ds_read_b64_tr_b16 v[164:165], v184 offset:0x8000
	ds_read_b64_tr_b16 v[166:167], v184 offset:0x8800
	ds_read_b64_tr_b16 v[170:171], v184 offset:0x9000
	ds_read_b64_tr_b16 v[172:173], v184 offset:0x9800
	ds_read_b64_tr_b16 v[174:175], v184 offset:0xa000
	ds_read_b64_tr_b16 v[176:177], v184 offset:0xa800
	ds_read_b64_tr_b16 v[178:179], v184 offset:0xb000
	ds_read_b64_tr_b16 v[180:181], v184 offset:0xb800
	s_waitcnt lgkmcnt(0)
	v_mfma_f32_32x32x16_f16 v[64:79], v[82:85], v[164:167], v[64:79]
	s_nop 0
	v_exp_f32_e32 v169, v112
	v_mfma_f32_32x32x16_f16 v[64:79], v[86:89], v[170:173], v[64:79]
	v_exp_f32_e32 v170, v113
	ds_read_b64_tr_b16 v[112:113], v184 offset:0x8200
	v_exp_f32_e32 v171, v114
	v_exp_f32_e32 v172, v115
	ds_read_b64_tr_b16 v[114:115], v184 offset:0x8a00
	ds_read_b64_tr_b16 v[164:165], v184 offset:0x9200
	ds_read_b64_tr_b16 v[166:167], v184 offset:0x9a00
	v_mfma_f32_32x32x16_f16 v[64:79], v[90:93], v[174:177], v[64:79]
	ds_read_b64_tr_b16 v[210:211], v184 offset:0xa200
	ds_read_b64_tr_b16 v[212:213], v184 offset:0xaa00
	ds_read_b64_tr_b16 v[214:215], v184 offset:0xb200
	ds_read_b64_tr_b16 v[216:217], v184 offset:0xba00
	v_mfma_f32_32x32x16_f16 v[64:79], v[160:163], v[178:181], v[64:79]
	s_waitcnt lgkmcnt(0)
	v_mfma_f32_32x32x16_f16 v[48:63], v[82:85], v[112:115], v[48:63]
	ds_read_b64_tr_b16 v[112:113], v184 offset:0x8400
	ds_read_b64_tr_b16 v[114:115], v184 offset:0x8c00
	v_exp_f32_e32 v173, v116
	v_exp_f32_e32 v174, v117
	ds_read_b64_tr_b16 v[116:117], v184 offset:0x9400
	v_exp_f32_e32 v175, v118
	v_exp_f32_e32 v176, v119
	v_mfma_f32_32x32x16_f16 v[48:63], v[86:89], v[164:167], v[48:63]
	ds_read_b64_tr_b16 v[118:119], v184 offset:0x9c00
	ds_read_b64_tr_b16 v[164:165], v184 offset:0xa400
	ds_read_b64_tr_b16 v[166:167], v184 offset:0xac00
	v_mfma_f32_32x32x16_f16 v[48:63], v[90:93], v[210:213], v[48:63]
	ds_read_b64_tr_b16 v[210:211], v184 offset:0xb400
	ds_read_b64_tr_b16 v[212:213], v184 offset:0xbc00
	v_mfma_f32_32x32x16_f16 v[48:63], v[160:163], v[214:217], v[48:63]
	s_waitcnt lgkmcnt(0)
	v_mfma_f32_32x32x16_f16 v[32:47], v[82:85], v[112:115], v[32:47]
	ds_read_b64_tr_b16 v[112:113], v184 offset:0x8600
	ds_read_b64_tr_b16 v[114:115], v184 offset:0x8e00
	v_exp_f32_e32 v177, v120
	v_exp_f32_e32 v178, v121
	v_exp_f32_e32 v179, v122
	v_exp_f32_e32 v180, v123
	v_mfma_f32_32x32x16_f16 v[32:47], v[86:89], v[116:119], v[32:47]
	ds_read_b64_tr_b16 v[116:117], v184 offset:0x9600
	ds_read_b64_tr_b16 v[118:119], v184 offset:0x9e00
	ds_read_b64_tr_b16 v[120:121], v184 offset:0xa600
	ds_read_b64_tr_b16 v[122:123], v184 offset:0xae00
	v_mfma_f32_32x32x16_f16 v[32:47], v[90:93], v[164:167], v[32:47]
	ds_read_b64_tr_b16 v[164:165], v184 offset:0xb600
	ds_read_b64_tr_b16 v[166:167], v184 offset:0xbe00
	v_mfma_f32_32x32x16_f16 v[32:47], v[160:163], v[210:213], v[32:47]
	s_waitcnt lgkmcnt(0)
	v_mfma_f32_32x32x16_f16 v[16:31], v[82:85], v[112:115], v[16:31]
	v_exp_f32_e32 v181, v124
	v_exp_f32_e32 v182, v125
	v_exp_f32_e32 v183, v126
	v_exp_f32_e32 v185, v127
	s_waitcnt vmcnt(0) lgkmcnt(0)
	s_barrier
	v_mfma_f32_32x32x16_f16 v[16:31], v[86:89], v[116:119], v[16:31]
	v_mfma_f32_32x32x16_f16 v[16:31], v[90:93], v[120:123], v[16:31]
	v_mfma_f32_32x32x16_f16 v[16:31], v[160:163], v[164:167], v[16:31]
	s_add_i32 s99, s99, 2
	s_add_i32 s4, s4, 0x10000
	s_add_i32 s5, s5, 4
	s_cmp_le_u32 s5, s33
	s_cbranch_scc1 .LBB3_44
	s_cmp_gt_u32 s99, s33
	s_cbranch_scc0 .LBB3_47
	s_branch .LBB3_60
